# v26: v24 + one static s_setprio 1 at entry for the younger waves (tid>=256) of both k_nca kernels
# baseline (speedup 1.0000x reference)
_Z5k_ncaILi0EEvPKDF16_S1_PKfS3_PDF16_S3_S3_S3_S3_Pf:
	s_load_dwordx4 s[12:15], s[0:1], 0x0
	v_readfirstlane_b32 s3, v0
	s_cmpk_ge_u32 s3, 0x100
	s_cbranch_scc0 .Lyw_prio_skip0
	s_setprio 1
.Lyw_prio_skip0:
	s_lshl_b32 s3, s2, 1
	s_and_b32 s3, s3, 12
	s_lshr_b32 s4, s2, 6
	v_lshrrev_b32_e32 v1, 5, v0
	s_add_i32 s3, s3, s4
	s_lshl_b32 s4, s2, 6
	v_and_b32_e32 v62, 4, v1
	v_lshrrev_b32_e32 v1, 4, v0
	s_and_b32 s4, s4, 64
	s_and_b32 s2, s2, 56
	v_and_b32_e32 v63, 4, v1
	v_bfe_u32 v1, v0, 2, 2
	s_lshl_b32 s20, s3, 3
	s_or_b32 s21, s4, s2
	v_or3_b32 v2, v62, s20, v1
	v_and_b32_e32 v61, 3, v0
	v_lshl_or_b32 v2, v2, 7, s21
	v_or3_b32 v2, v2, v63, v61
	s_movk_i32 s4, 0x48
	v_mul_lo_u32 v54, v2, s4
	v_mov_b32_e32 v55, 0
	s_waitcnt lgkmcnt(0)
	v_lshl_add_u64 v[6:7], v[54:55], 1, s[12:13]
	v_and_b32_e32 v2, 48, v0
	v_mov_b32_e32 v3, v55
	v_lshl_add_u64 v[8:9], v[6:7], 0, v[2:3]
	global_load_dwordx4 v[2:5], v[8:9], off offset:64
	global_load_dwordx4 v[10:13], v[8:9], off
	global_load_dwordx4 v[22:25], v[6:7], off offset:128
	v_mul_u32_u24_e32 v6, 0x1c72, v0
	v_mul_u32_u24_e32 v65, 0x195, v0
	s_movk_i32 s2, 0xffee
	s_add_i32 s20, s20, -5
	s_add_i32 s21, s21, -5
	v_lshrrev_b32_e32 v64, 16, v6
	v_mul_i32_i24_sdwa v6, v65, s2 dst_sel:DWORD dst_unused:UNUSED_PAD src0_sel:WORD_1 src1_sel:DWORD
	v_add_u32_sdwa v14, s20, v65 dst_sel:DWORD dst_unused:UNUSED_PAD src0_sel:DWORD src1_sel:WORD_1
	v_add3_u32 v15, s21, v64, v6
	v_or_b32_e32 v6, v15, v14
	s_movk_i32 s5, 0x80
	v_cmp_gt_u32_e32 vcc, s5, v6
	v_mov_b64_e32 v[6:7], 0
	v_mov_b64_e32 v[8:9], 0
	s_and_saveexec_b64 s[2:3], vcc
	v_lshl_or_b32 v9, v14, 7, v15
	v_mad_i32_i24 v8, v64, -9, v0
	v_mul_lo_u32 v9, v9, s4
	v_lshl_add_u32 v8, v8, 3, v9
	v_ashrrev_i32_e32 v9, 31, v8
	s_or_b64 exec, exec, s[2:3]
	v_lshl_add_u64 v[8:9], v[8:9], 1, s[14:15]
	global_load_dwordx4 v[26:29], v[8:9], off
	v_or_b32_e32 v59, 0x200, v0
	v_mul_u32_u24_e32 v8, 0x1c72, v59
	v_lshrrev_b32_e32 v66, 16, v8
	v_mul_u32_u24_e32 v8, 0x653, v59
	v_lshrrev_b32_e32 v67, 18, v8
	v_mul_i32_i24_e32 v9, 0xffffffee, v67
	v_add_u32_e32 v8, s20, v67
	v_add3_u32 v9, s21, v66, v9
	v_or_b32_e32 v14, v9, v8
	v_cmp_gt_u32_e64 s[2:3], s5, v14
	s_and_saveexec_b64 s[4:5], s[2:3]
	v_lshl_or_b32 v7, v8, 7, v9
	s_movk_i32 s6, 0x48
	v_mad_i32_i24 v6, v66, -9, v59
	v_mul_lo_u32 v7, v7, s6
	v_lshl_add_u32 v6, v6, 3, v7
	v_ashrrev_i32_e32 v7, 31, v6
	s_or_b64 exec, exec, s[4:5]
	v_lshl_add_u64 v[6:7], v[6:7], 1, s[14:15]
	global_load_dwordx4 v[30:33], v[6:7], off
	v_or_b32_e32 v58, 0x400, v0
	v_mul_u32_u24_e32 v6, 0x1c72, v58
	v_lshrrev_b32_e32 v68, 16, v6
	v_mul_u32_u24_e32 v6, 0x653, v58
	v_lshrrev_b32_e32 v69, 18, v6
	v_mul_i32_i24_e32 v6, 0xffffffee, v69
	v_add_u32_e32 v14, s20, v69
	v_add3_u32 v15, s21, v68, v6
	v_or_b32_e32 v6, v15, v14
	s_movk_i32 s8, 0x80
	v_cmp_gt_u32_e64 s[4:5], s8, v6
	v_mov_b64_e32 v[6:7], 0
	v_mov_b64_e32 v[8:9], 0
	s_and_saveexec_b64 s[6:7], s[4:5]
	v_lshl_or_b32 v9, v14, 7, v15
	s_movk_i32 s9, 0x48
	v_mad_i32_i24 v8, v68, -9, v58
	v_mul_lo_u32 v9, v9, s9
	v_lshl_add_u32 v8, v8, 3, v9
	v_mov_b32_e32 v9, 0
	s_or_b64 exec, exec, s[6:7]
	v_lshl_add_u64 v[8:9], v[8:9], 1, s[14:15]
	global_load_dwordx4 v[34:37], v[8:9], off
	v_or_b32_e32 v70, 0x600, v0
	v_mul_u32_u24_e32 v8, 0x1c72, v70
	v_lshrrev_b32_e32 v71, 16, v8
	v_mul_u32_u24_e32 v8, 0x653, v70
	v_lshrrev_b32_e32 v72, 18, v8
	v_mul_i32_i24_e32 v9, 0xffffffee, v72
	v_add_u32_e32 v8, s20, v72
	v_add3_u32 v9, s21, v71, v9
	v_or_b32_e32 v14, v9, v8
	v_cmp_gt_u32_e64 s[8:9], s8, v14
	s_and_saveexec_b64 s[6:7], s[8:9]
	v_lshl_or_b32 v7, v8, 7, v9
	s_movk_i32 s10, 0x48
	v_mad_i32_i24 v6, v71, -9, v70
	v_mul_lo_u32 v7, v7, s10
	v_lshl_add_u32 v6, v6, 3, v7
	v_mov_b32_e32 v7, 0
	s_or_b64 exec, exec, s[6:7]
	v_lshl_add_u64 v[6:7], v[6:7], 1, s[14:15]
	global_load_dwordx4 v[42:45], v[6:7], off
	v_or_b32_e32 v73, 0x800, v0
	v_mul_u32_u24_e32 v6, 0x1c72, v73
	v_lshrrev_b32_e32 v14, 16, v6
	v_mul_u32_u24_e32 v6, 0xca5, v73
	s_load_dwordx2 s[12:13], s[0:1], 0x18
	v_lshrrev_b32_e32 v6, 19, v6
	v_mul_i32_i24_e32 v7, 0xffffffee, v6
	v_add_u32_e32 v15, s20, v6
	v_add3_u32 v16, s21, v14, v7
	v_or_b32_e32 v6, v16, v15
	s_movk_i32 s18, 0x80
	v_cmp_gt_u32_e64 s[10:11], s18, v6
	v_mov_b64_e32 v[6:7], 0
	v_mov_b64_e32 v[8:9], 0
	s_and_saveexec_b64 s[6:7], s[10:11]
	v_lshl_or_b32 v9, v15, 7, v16
	s_movk_i32 s16, 0x48
	v_mad_i32_i24 v8, v14, -9, v73
	v_mul_lo_u32 v9, v9, s16
	v_lshl_add_u32 v8, v8, 3, v9
	v_mov_b32_e32 v9, 0
	s_or_b64 exec, exec, s[6:7]
	v_lshl_add_u64 v[8:9], v[8:9], 1, s[14:15]
	global_load_dwordx4 v[46:49], v[8:9], off
	v_or_b32_e32 v74, 0xa00, v0
	v_min_u32_e32 v8, 0xb63, v74
	v_mul_u32_u24_e32 v14, 0xca5, v8
	s_load_dwordx2 s[16:17], s[0:1], 0x10
	s_load_dwordx2 s[64:65], s[0:1], 0x20
	v_mul_u32_u24_e32 v9, 0x1c72, v8
	v_lshrrev_b32_e32 v14, 19, v14
	v_lshrrev_b32_e32 v9, 16, v9
	v_mul_i32_i24_e32 v15, 0xffffffee, v14
	v_add_u32_e32 v14, s20, v14
	v_add3_u32 v15, s21, v9, v15
	v_or_b32_e32 v16, v15, v14
	v_cmp_gt_u32_e64 s[6:7], s18, v16
	s_and_saveexec_b64 s[18:19], s[6:7]
	v_lshl_or_b32 v7, v14, 7, v15
	s_movk_i32 s22, 0x48
	v_mad_i32_i24 v6, v9, -9, v8
	v_mul_lo_u32 v7, v7, s22
	v_lshl_add_u32 v6, v6, 3, v7
	v_mov_b32_e32 v7, 0
	s_or_b64 exec, exec, s[18:19]
	v_lshl_add_u64 v[6:7], v[6:7], 1, s[14:15]
	s_movk_i32 s14, 0xe39
	global_load_dwordx4 v[38:41], v[6:7], off
	v_mul_u32_u24_sdwa v6, v0, s14 dst_sel:DWORD dst_unused:UNUSED_PAD src0_sel:WORD_0 src1_sel:DWORD
	v_lshrrev_b32_e32 v60, 16, v6
	v_or_b32_e32 v14, 0x200, v0
	s_movk_i32 s14, 0xffee
	s_movk_i32 s15, 0x48
	v_mul_u32_u24_e32 v6, 0x48, v60
	v_mul_u32_u24_e32 v8, 0xe39, v14
	v_mad_i32_i24 v52, v60, s14, v0
	v_lshlrev_b32_e32 v50, 2, v6
	v_mov_b32_e32 v51, 0
	v_mul_i32_i24_sdwa v15, v8, s14 dst_sel:DWORD dst_unused:UNUSED_PAD src0_sel:WORD_1 src1_sel:DWORD
	v_mul_u32_u24_sdwa v8, v8, s15 dst_sel:DWORD dst_unused:UNUSED_PAD src0_sel:WORD_1 src1_sel:DWORD
	s_waitcnt lgkmcnt(0)
	v_lshl_add_u64 v[6:7], s[16:17], 0, v[50:51]
	v_lshlrev_b32_e32 v56, 2, v52
	v_lshlrev_b32_e32 v50, 2, v8
	v_add_lshl_u32 v14, v15, v14, 2
	v_ashrrev_i32_e32 v57, 31, v56
	v_lshl_add_u64 v[8:9], s[16:17], 0, v[50:51]
	v_ashrrev_i32_e32 v15, 31, v14
	v_lshl_add_u64 v[6:7], v[56:57], 2, v[6:7]
	v_lshl_add_u64 v[8:9], v[14:15], 2, v[8:9]
	global_load_dwordx4 v[18:21], v[6:7], off
	global_load_dwordx4 v[14:17], v[8:9], off
	v_min_u32_e32 v8, 0x50f, v58
	v_mul_u32_u24_e32 v6, 0xe39, v8
	v_mul_i32_i24_sdwa v9, v6, s14 dst_sel:DWORD dst_unused:UNUSED_PAD src0_sel:WORD_1 src1_sel:DWORD
	v_mul_u32_u24_sdwa v6, v6, s15 dst_sel:DWORD dst_unused:UNUSED_PAD src0_sel:WORD_1 src1_sel:DWORD
	v_lshlrev_b32_e32 v50, 2, v6
	v_add_lshl_u32 v8, v9, v8, 2
	v_lshl_add_u64 v[6:7], s[16:17], 0, v[50:51]
	v_ashrrev_i32_e32 v9, 31, v8
	v_min_u32_e32 v50, 0x47, v0
	v_lshl_add_u64 v[6:7], v[8:9], 2, v[6:7]
	v_lshlrev_b32_e32 v50, 2, v50
	global_load_dwordx4 v[6:9], v[6:7], off
	s_nop 0
	global_load_dword v57, v50, s[12:13]
	s_movk_i32 s12, 0x144
	v_cmp_gt_u32_e64 s[12:13], s12, v0
	s_and_saveexec_b64 s[14:15], s[12:13]
	s_cbranch_execz .LBB1_14
	v_mul_i32_i24_e32 v50, 0x1c72, v52
	v_lshrrev_b32_e32 v53, 31, v50
	v_add_u16_sdwa v50, v50, v53 dst_sel:DWORD dst_unused:UNUSED_PAD src0_sel:WORD_1 src1_sel:DWORD
	v_bfe_i32 v50, v50, 0, 16
	v_mul_i32_i24_e32 v53, -9, v50
	v_mad_u32_u24 v50, v60, 20, v50
	v_mul_i32_i24_e32 v50, 0xa0, v50
	v_add_lshl_u32 v52, v53, v52, 4
	v_add3_u32 v75, v50, 0, v52
	v_mov_b32_e32 v50, v51
	v_mov_b32_e32 v52, v51
	v_mov_b32_e32 v53, v51
	ds_write_b128 v75, v[50:53] offset:2880

_Z5k_ncaILi1EEvPKDF16_S1_PKfS3_PDF16_S3_S3_S3_S3_Pf:
	s_load_dwordx4 s[20:23], s[0:1], 0x0
	v_readfirstlane_b32 s3, v0
	s_cmpk_ge_u32 s3, 0x100
	s_cbranch_scc0 .Lyw_prio_skip1
	s_setprio 1
.Lyw_prio_skip1:
	s_lshl_b32 s3, s2, 1
	s_and_b32 s3, s3, 12
	s_lshr_b32 s4, s2, 6
	s_add_i32 s3, s3, s4
	v_lshrrev_b32_e32 v1, 5, v0
	s_lshl_b32 s4, s2, 6
	v_and_b32_e32 v76, 4, v1
	s_lshl_b32 s29, s3, 3
	s_and_b32 s4, s4, 64
	s_and_b32 s2, s2, 56
	v_bfe_u32 v60, v0, 2, 2
	v_or_b32_e32 v58, s29, v76
	s_or_b32 s28, s4, s2
	v_lshrrev_b32_e32 v52, 4, v0
	v_or_b32_e32 v2, v58, v60
	v_and_b32_e32 v57, 4, v52
	v_and_b32_e32 v1, 3, v0
	v_lshl_or_b32 v2, v2, 7, s28
	v_or3_b32 v56, v2, v57, v1
	s_movk_i32 s4, 0x48
	v_mul_lo_u32 v2, v56, s4
	v_mov_b32_e32 v3, 0
	s_waitcnt lgkmcnt(0)
	v_lshl_add_u64 v[6:7], v[2:3], 1, s[20:21]
	v_and_b32_e32 v2, 48, v0
	v_lshl_add_u64 v[8:9], v[6:7], 0, v[2:3]
	global_load_dwordx4 v[2:5], v[8:9], off offset:64
	global_load_dwordx4 v[10:13], v[8:9], off
	global_load_dwordx4 v[22:25], v[6:7], off offset:128
	v_mul_u32_u24_e32 v6, 0x1c72, v0
	v_mul_u32_u24_e32 v78, 0x195, v0
	s_movk_i32 s2, 0xffee
	s_add_i32 s29, s29, -5
	s_add_i32 s30, s28, -5
	v_lshrrev_b32_e32 v77, 16, v6
	v_mul_i32_i24_sdwa v6, v78, s2 dst_sel:DWORD dst_unused:UNUSED_PAD src0_sel:WORD_1 src1_sel:DWORD
	v_add_u32_sdwa v14, s29, v78 dst_sel:DWORD dst_unused:UNUSED_PAD src0_sel:DWORD src1_sel:WORD_1
	v_add3_u32 v15, s30, v77, v6
	v_or_b32_e32 v6, v15, v14
	s_movk_i32 s5, 0x80
	v_cmp_gt_u32_e32 vcc, s5, v6
	v_mov_b64_e32 v[6:7], 0
	v_mov_b64_e32 v[8:9], 0
	s_and_saveexec_b64 s[2:3], vcc
	v_lshl_or_b32 v9, v14, 7, v15
	v_mad_i32_i24 v8, v77, -9, v0
	v_mul_lo_u32 v9, v9, s4
	v_lshl_add_u32 v8, v8, 3, v9
	v_ashrrev_i32_e32 v9, 31, v8
	s_or_b64 exec, exec, s[2:3]
	v_lshl_add_u64 v[8:9], v[8:9], 1, s[22:23]
	global_load_dwordx4 v[26:29], v[8:9], off
	v_or_b32_e32 v62, 0x200, v0
	v_mul_u32_u24_e32 v8, 0x1c72, v62
	v_lshrrev_b32_e32 v79, 16, v8
	v_mul_u32_u24_e32 v8, 0x653, v62
	v_lshrrev_b32_e32 v80, 18, v8
	v_mul_i32_i24_e32 v9, 0xffffffee, v80
	v_add_u32_e32 v8, s29, v80
	v_add3_u32 v9, s30, v79, v9
	v_or_b32_e32 v14, v9, v8
	v_cmp_gt_u32_e64 s[2:3], s5, v14
	s_and_saveexec_b64 s[4:5], s[2:3]
	v_lshl_or_b32 v7, v8, 7, v9
	s_movk_i32 s6, 0x48
	v_mad_i32_i24 v6, v79, -9, v62
	v_mul_lo_u32 v7, v7, s6
	v_lshl_add_u32 v6, v6, 3, v7
	v_ashrrev_i32_e32 v7, 31, v6
	s_or_b64 exec, exec, s[4:5]
	v_lshl_add_u64 v[6:7], v[6:7], 1, s[22:23]
	global_load_dwordx4 v[30:33], v[6:7], off
	v_or_b32_e32 v61, 0x400, v0
	v_mul_u32_u24_e32 v6, 0x1c72, v61
	v_lshrrev_b32_e32 v81, 16, v6
	v_mul_u32_u24_e32 v6, 0x653, v61
	v_lshrrev_b32_e32 v82, 18, v6
	v_mul_i32_i24_e32 v6, 0xffffffee, v82
	v_add_u32_e32 v14, s29, v82
	v_add3_u32 v15, s30, v81, v6
	v_or_b32_e32 v6, v15, v14
	s_movk_i32 s8, 0x80
	v_cmp_gt_u32_e64 s[4:5], s8, v6
	v_mov_b64_e32 v[6:7], 0
	v_mov_b64_e32 v[8:9], 0
	s_and_saveexec_b64 s[6:7], s[4:5]
	v_lshl_or_b32 v9, v14, 7, v15
	s_movk_i32 s9, 0x48
	v_mad_i32_i24 v8, v81, -9, v61
	v_mul_lo_u32 v9, v9, s9
	v_lshl_add_u32 v8, v8, 3, v9
	v_mov_b32_e32 v9, 0
	s_or_b64 exec, exec, s[6:7]
	v_lshl_add_u64 v[8:9], v[8:9], 1, s[22:23]
	global_load_dwordx4 v[34:37], v[8:9], off
	v_or_b32_e32 v83, 0x600, v0
	v_mul_u32_u24_e32 v8, 0x1c72, v83
	v_lshrrev_b32_e32 v84, 16, v8
	v_mul_u32_u24_e32 v8, 0x653, v83
	v_lshrrev_b32_e32 v85, 18, v8
	v_mul_i32_i24_e32 v9, 0xffffffee, v85
	v_add_u32_e32 v8, s29, v85
	v_add3_u32 v9, s30, v84, v9
	v_or_b32_e32 v14, v9, v8
	v_cmp_gt_u32_e64 s[8:9], s8, v14
	s_and_saveexec_b64 s[6:7], s[8:9]
	v_lshl_or_b32 v7, v8, 7, v9
	s_movk_i32 s10, 0x48
	v_mad_i32_i24 v6, v84, -9, v83
	v_mul_lo_u32 v7, v7, s10
	v_lshl_add_u32 v6, v6, 3, v7
	v_mov_b32_e32 v7, 0
	s_or_b64 exec, exec, s[6:7]
	v_lshl_add_u64 v[6:7], v[6:7], 1, s[22:23]
	global_load_dwordx4 v[42:45], v[6:7], off
	v_or_b32_e32 v86, 0x800, v0
	v_mul_u32_u24_e32 v6, 0x1c72, v86
	v_lshrrev_b32_e32 v14, 16, v6
	v_mul_u32_u24_e32 v6, 0xca5, v86
	s_load_dwordx8 s[12:19], s[0:1], 0x28
	s_load_dwordx2 s[20:21], s[0:1], 0x18
	v_lshrrev_b32_e32 v6, 19, v6
	v_mul_i32_i24_e32 v7, 0xffffffee, v6
	v_add_u32_e32 v15, s29, v6
	v_add3_u32 v16, s30, v14, v7
	v_or_b32_e32 v6, v16, v15
	s_movk_i32 s26, 0x80
	v_cmp_gt_u32_e64 s[10:11], s26, v6
	v_mov_b64_e32 v[6:7], 0
	v_mov_b64_e32 v[8:9], 0
	s_and_saveexec_b64 s[6:7], s[10:11]
	v_lshl_or_b32 v9, v15, 7, v16
	s_movk_i32 s24, 0x48
	v_mad_i32_i24 v8, v14, -9, v86
	v_mul_lo_u32 v9, v9, s24
	v_lshl_add_u32 v8, v8, 3, v9
	v_mov_b32_e32 v9, 0
	s_or_b64 exec, exec, s[6:7]
	v_lshl_add_u64 v[8:9], v[8:9], 1, s[22:23]
	global_load_dwordx4 v[46:49], v[8:9], off
	v_or_b32_e32 v87, 0xa00, v0
	v_min_u32_e32 v8, 0xb63, v87
	v_mul_u32_u24_e32 v14, 0xca5, v8
	s_load_dwordx2 s[24:25], s[0:1], 0x10
	s_load_dwordx2 s[64:65], s[0:1], 0x48
	v_mul_u32_u24_e32 v9, 0x1c72, v8
	v_lshrrev_b32_e32 v14, 19, v14
	v_lshrrev_b32_e32 v9, 16, v9
	v_mul_i32_i24_e32 v15, 0xffffffee, v14
	v_add_u32_e32 v14, s29, v14
	v_add3_u32 v15, s30, v9, v15
	v_or_b32_e32 v16, v15, v14
	v_and_b32_e32 v59, 15, v0
	v_cmp_gt_u32_e64 s[6:7], s26, v16
	s_and_saveexec_b64 s[26:27], s[6:7]
	v_lshl_or_b32 v7, v14, 7, v15
	s_movk_i32 s31, 0x48
	v_mad_i32_i24 v6, v9, -9, v8
	v_mul_lo_u32 v7, v7, s31
	v_lshl_add_u32 v6, v6, 3, v7
	v_mov_b32_e32 v7, 0
	s_or_b64 exec, exec, s[26:27]
	v_lshl_add_u64 v[6:7], v[6:7], 1, s[22:23]
	s_movk_i32 s22, 0xe39
	global_load_dwordx4 v[38:41], v[6:7], off
	v_mul_u32_u24_sdwa v6, v0, s22 dst_sel:DWORD dst_unused:UNUSED_PAD src0_sel:WORD_0 src1_sel:DWORD
	v_lshrrev_b32_e32 v75, 16, v6
	v_or_b32_e32 v14, 0x200, v0
	s_movk_i32 s22, 0xffee
	s_movk_i32 s23, 0x48
	v_mul_u32_u24_e32 v6, 0x48, v75
	v_mul_u32_u24_e32 v8, 0xe39, v14
	v_mad_i32_i24 v53, v75, s22, v0
	v_lshlrev_b32_e32 v50, 2, v6
	v_mov_b32_e32 v51, 0
	v_mul_i32_i24_sdwa v15, v8, s22 dst_sel:DWORD dst_unused:UNUSED_PAD src0_sel:WORD_1 src1_sel:DWORD
	v_mul_u32_u24_sdwa v8, v8, s23 dst_sel:DWORD dst_unused:UNUSED_PAD src0_sel:WORD_1 src1_sel:DWORD
	s_waitcnt lgkmcnt(0)
	v_lshl_add_u64 v[6:7], s[24:25], 0, v[50:51]
	v_lshlrev_b32_e32 v54, 2, v53
	v_lshlrev_b32_e32 v50, 2, v8
	v_add_lshl_u32 v14, v15, v14, 2
	v_ashrrev_i32_e32 v55, 31, v54
	v_lshl_add_u64 v[8:9], s[24:25], 0, v[50:51]
	v_ashrrev_i32_e32 v15, 31, v14
	v_lshl_add_u64 v[6:7], v[54:55], 2, v[6:7]
	v_lshl_add_u64 v[8:9], v[14:15], 2, v[8:9]
	global_load_dwordx4 v[18:21], v[6:7], off
	global_load_dwordx4 v[14:17], v[8:9], off
	v_min_u32_e32 v8, 0x50f, v61
	v_mul_u32_u24_e32 v6, 0xe39, v8
	v_mul_i32_i24_sdwa v9, v6, s22 dst_sel:DWORD dst_unused:UNUSED_PAD src0_sel:WORD_1 src1_sel:DWORD
	v_mul_u32_u24_sdwa v6, v6, s23 dst_sel:DWORD dst_unused:UNUSED_PAD src0_sel:WORD_1 src1_sel:DWORD
	v_lshlrev_b32_e32 v50, 2, v6
	v_lshl_add_u64 v[6:7], s[24:25], 0, v[50:51]
	v_min_u32_e32 v50, 0x47, v0
	v_add_lshl_u32 v8, v9, v8, 2
	v_lshlrev_b32_e32 v50, 2, v50
	v_add_u32_e32 v63, -8, v59
	v_ashrrev_i32_e32 v9, 31, v8
	global_load_dword v68, v50, s[20:21]
	v_min_u32_e32 v50, 6, v59
	v_med3_i32 v64, v63, 0, 2
	v_mul_u32_u24_e32 v52, 7, v52
	v_and_b32_e32 v72, 15, v62
	v_lshl_add_u64 v[6:7], v[8:9], 2, v[6:7]
	v_lshlrev_b32_e32 v55, 2, v50
	v_lshlrev_b32_e32 v65, 2, v64
	v_add_lshl_u32 v50, v52, v50, 2
	v_lshrrev_b32_e32 v52, 4, v62
	v_add_u32_e32 v71, -8, v72
	global_load_dwordx4 v[6:9], v[6:7], off
	v_med3_i32 v67, v71, 0, 2
	global_load_dword v55, v55, s[14:15]
	s_nop 0
	global_load_dword v64, v65, s[18:19]
	global_load_dword v70, v65, s[16:17]
	v_min_u32_e32 v65, 6, v72
	v_mul_u32_u24_e32 v52, 7, v52
	v_add_lshl_u32 v52, v52, v65, 2
	global_load_dword v66, v50, s[12:13]
	global_load_dword v65, v52, s[12:13]
	v_mad_u32_u24 v50, 64, 3, v67
	v_add_u32_e32 v50, 0xffffff40, v50
	v_lshl_add_u64 v[88:89], v[50:51], 2, s[16:17]
	v_min_u32_e32 v50, 0x47f, v61
	v_lshrrev_b32_e32 v52, 4, v50
	v_and_b32_e32 v50, 15, v50
	v_add_u32_e32 v69, -8, v50
	s_movk_i32 s14, 0xff40
	v_min_u32_e32 v67, 6, v50
	v_med3_i32 v50, v69, 0, 2
	v_mul_u32_u24_e32 v52, 3, v52
	v_add3_u32 v50, v52, v50, s14
	global_load_dword v74, v[88:89], off
	v_lshlrev_b32_e32 v67, 2, v67
	v_lshl_add_u64 v[88:89], v[50:51], 2, s[16:17]
	global_load_dword v67, v67, s[12:13] offset:1764
	s_movk_i32 s12, 0x144
	global_load_dword v73, v[88:89], off
	v_cmp_gt_u32_e64 s[12:13], s12, v0
	s_and_saveexec_b64 s[14:15], s[12:13]
	s_cbranch_execz .LBB2_14
	v_mul_i32_i24_e32 v50, 0x1c72, v53
	v_lshrrev_b32_e32 v52, 31, v50
	v_add_u16_sdwa v50, v50, v52 dst_sel:DWORD dst_unused:UNUSED_PAD src0_sel:WORD_1 src1_sel:DWORD
	v_bfe_i32 v50, v50, 0, 16
	v_mul_i32_i24_e32 v52, -9, v50
	v_mad_u32_u24 v50, v75, 20, v50
	v_mul_i32_i24_e32 v50, 0xa0, v50
	v_add_lshl_u32 v52, v52, v53, 4
	v_add3_u32 v88, v50, 0, v52
	v_mov_b32_e32 v50, v51
	v_mov_b32_e32 v52, v51
	v_mov_b32_e32 v53, v51
	ds_write_b128 v88, v[50:53] offset:2880
